# E24: E21 + nt on bf16 stores of every MoE weight-conversion site (GEMM tails, converter WGs), as already in mix
# speedup vs baseline: 1.0112x; 1.0001x over previous
.LBB0_686:
	ds_write2_b32 v84, v34, v35 offset1:1
	ds_write2_b32 v84, v36, v37 offset0:2 offset1:3
	ds_write2_b32 v85, v38, v39 offset1:1
	ds_write2_b32 v86, v40, v41 offset1:1
	ds_write2_b32 v87, v42, v43 offset1:1
	ds_write2_b32 v88, v44, v45 offset1:1
	ds_write2_b32 v89, v46, v47 offset1:1
	ds_write2_b32 v90, v48, v49 offset1:1
	ds_write2_b32 v91, v54, v55 offset1:1
	ds_write2_b32 v92, v56, v57 offset1:1
	ds_write2_b32 v93, v50, v51 offset1:1
	ds_write2_b32 v94, v52, v53 offset1:1
	ds_write2_b32 v95, v62, v63 offset1:1
	ds_write2_b32 v96, v64, v65 offset1:1
	ds_write2_b32 v97, v58, v59 offset1:1
	ds_write2_b32 v98, v60, v61 offset1:1
	s_waitcnt lgkmcnt(0)
	ds_read2_b32 v[92:93], v83 offset0:33 offset1:41
	ds_read2_b32 v[94:95], v83 offset1:8
	ds_read2_b32 v[96:97], v83 offset0:66 offset1:74
	ds_read2_b32 v[98:99], v83 offset0:99 offset1:107
	ds_read2_b32 v[102:103], v83 offset0:132 offset1:140
	ds_read2_b32 v[104:105], v83 offset0:165 offset1:173
	ds_read2_b32 v[106:107], v83 offset0:198 offset1:206
	ds_read2_b32 v[108:109], v83 offset0:231 offset1:239
	v_lshl_add_u64 v[90:91], s[2:3], 0, v[100:101]
	s_waitcnt lgkmcnt(6)
	v_cvt_pk_bf16_f32 v86, v94, v92
	s_waitcnt lgkmcnt(4)
	v_cvt_pk_bf16_f32 v87, v96, v98
	s_waitcnt lgkmcnt(2)
	v_cvt_pk_bf16_f32 v88, v102, v104
	s_waitcnt lgkmcnt(0)
	v_cvt_pk_bf16_f32 v89, v106, v108
	v_lshl_add_u64 v[110:111], v[90:91], 0, v[70:71]
	global_store_dwordx4 v[110:111], v[86:89], off nt
	v_lshl_add_u64 v[110:111], v[90:91], 0, v[74:75]
	s_add_i32 s26, s26, 16
	v_cvt_pk_bf16_f32 v86, v95, v93
	v_cvt_pk_bf16_f32 v87, v97, v99
	v_cvt_pk_bf16_f32 v88, v103, v105
	v_cvt_pk_bf16_f32 v89, v107, v109
	v_lshl_add_u64 v[92:93], v[90:91], 0, v[72:73]
	global_store_dwordx4 v[92:93], v[86:89], off nt
	ds_read2_b32 v[92:93], v83 offset0:49 offset1:57
	ds_read2_b32 v[94:95], v83 offset0:16 offset1:24
	ds_read2_b32 v[96:97], v83 offset0:82 offset1:90
	ds_read2_b32 v[98:99], v83 offset0:115 offset1:123
	ds_read2_b32 v[102:103], v83 offset0:148 offset1:156
	ds_read2_b32 v[104:105], v83 offset0:181 offset1:189
	ds_read2_b32 v[106:107], v83 offset0:214 offset1:222
	ds_read2_b32 v[108:109], v83 offset0:247 offset1:255
	v_lshl_add_u64 v[90:91], v[90:91], 0, v[76:77]
	s_waitcnt lgkmcnt(6)
	v_cvt_pk_bf16_f32 v86, v94, v92
	s_waitcnt lgkmcnt(4)
	v_cvt_pk_bf16_f32 v87, v96, v98
	s_waitcnt lgkmcnt(2)
	v_cvt_pk_bf16_f32 v88, v102, v104
	s_waitcnt lgkmcnt(0)
	v_cvt_pk_bf16_f32 v89, v106, v108
	global_store_dwordx4 v[110:111], v[86:89], off nt
	s_addk_i32 s27, 0x200
	s_add_i32 s28, s28, 32
	v_cvt_pk_bf16_f32 v86, v95, v93
	v_cvt_pk_bf16_f32 v87, v97, v99
	v_cvt_pk_bf16_f32 v88, v103, v105
	v_cvt_pk_bf16_f32 v89, v107, v109
	global_store_dwordx4 v[90:91], v[86:89], off nt
	s_waitcnt lgkmcnt(0)
	s_cmp_ge_i32 s12, s25
	s_cselect_b64 s[4:5], -1, 0

.LBB0_698:
	v_add_u32_e32 v85, 0x420, v84
	v_add_u32_e32 v86, 0x428, v84
	v_add_u32_e32 v87, 0x840, v84
	v_add_u32_e32 v88, 0x848, v84
	v_add_u32_e32 v89, 0xc60, v84
	v_add_u32_e32 v90, 0xc68, v84
	v_add_u32_e32 v91, 0x1080, v84
	v_add_u32_e32 v92, 0x1088, v84
	v_add_u32_e32 v93, 0x14a0, v84
	v_add_u32_e32 v94, 0x14a8, v84
	v_add_u32_e32 v95, 0x18c0, v84
	v_add_u32_e32 v96, 0x18c8, v84
	v_add_u32_e32 v97, 0x1ce0, v84
	v_add_u32_e32 v98, 0x1ce8, v84
	s_waitcnt vmcnt(7)
	ds_write2_b32 v84, v2, v3 offset1:1
	ds_write2_b32 v84, v4, v5 offset0:2 offset1:3
	s_waitcnt vmcnt(6)
	ds_write2_b32 v85, v6, v7 offset1:1
	ds_write2_b32 v86, v8, v9 offset1:1
	s_waitcnt vmcnt(5)
	ds_write2_b32 v87, v10, v11 offset1:1
	ds_write2_b32 v88, v12, v13 offset1:1
	s_waitcnt vmcnt(4)
	ds_write2_b32 v89, v14, v15 offset1:1
	ds_write2_b32 v90, v16, v17 offset1:1
	s_waitcnt vmcnt(3)
	ds_write2_b32 v91, v18, v19 offset1:1
	ds_write2_b32 v92, v20, v21 offset1:1
	s_waitcnt vmcnt(2)
	ds_write2_b32 v93, v22, v23 offset1:1
	ds_write2_b32 v94, v24, v25 offset1:1
	s_waitcnt vmcnt(1)
	ds_write2_b32 v95, v26, v27 offset1:1
	ds_write2_b32 v96, v28, v29 offset1:1
	s_waitcnt vmcnt(0)
	ds_write2_b32 v97, v30, v31 offset1:1
	ds_write2_b32 v98, v32, v33 offset1:1
	s_waitcnt lgkmcnt(0)
	ds_read2_b32 v[106:107], v83 offset0:33 offset1:41
	ds_read2_b32 v[108:109], v83 offset1:8
	ds_read2_b32 v[110:111], v83 offset0:66 offset1:74
	ds_read2_b32 v[112:113], v83 offset0:99 offset1:107
	ds_read2_b32 v[114:115], v83 offset0:132 offset1:140
	ds_read2_b32 v[116:117], v83 offset0:165 offset1:173
	ds_read2_b32 v[118:119], v83 offset0:198 offset1:206
	ds_read2_b32 v[120:121], v83 offset0:231 offset1:239
	v_lshlrev_b32_e32 v100, 1, v68
	v_lshl_add_u64 v[122:123], s[0:1], 0, v[100:101]
	s_waitcnt lgkmcnt(6)
	v_cvt_pk_bf16_f32 v102, v108, v106
	s_waitcnt lgkmcnt(4)
	v_cvt_pk_bf16_f32 v103, v110, v112
	s_waitcnt lgkmcnt(2)
	v_cvt_pk_bf16_f32 v104, v114, v116
	s_waitcnt lgkmcnt(0)
	v_cvt_pk_bf16_f32 v105, v118, v120
	v_lshl_add_u64 v[124:125], v[122:123], 0, v[70:71]
	global_store_dwordx4 v[124:125], v[102:105], off nt
	s_andn2_b64 vcc, exec, s[4:5]
	s_mov_b64 s[4:5], -1
	v_cvt_pk_bf16_f32 v102, v109, v107
	v_cvt_pk_bf16_f32 v103, v111, v113
	v_cvt_pk_bf16_f32 v104, v115, v117
	v_cvt_pk_bf16_f32 v105, v119, v121
	ds_read2_b32 v[108:109], v83 offset0:49 offset1:57
	ds_read2_b32 v[110:111], v83 offset0:16 offset1:24
	ds_read2_b32 v[112:113], v83 offset0:82 offset1:90
	ds_read2_b32 v[114:115], v83 offset0:115 offset1:123
	ds_read2_b32 v[116:117], v83 offset0:148 offset1:156
	ds_read2_b32 v[118:119], v83 offset0:181 offset1:189
	ds_read2_b32 v[120:121], v83 offset0:214 offset1:222
	ds_read2_b32 v[124:125], v83 offset0:247 offset1:255
	v_lshl_add_u64 v[106:107], v[122:123], 0, v[72:73]
	global_store_dwordx4 v[106:107], v[102:105], off nt
	v_lshl_add_u64 v[106:107], v[122:123], 0, v[74:75]
	s_waitcnt lgkmcnt(6)
	v_cvt_pk_bf16_f32 v102, v110, v108
	s_waitcnt lgkmcnt(4)
	v_cvt_pk_bf16_f32 v103, v112, v114
	s_waitcnt lgkmcnt(2)
	v_cvt_pk_bf16_f32 v104, v116, v118
	s_waitcnt lgkmcnt(0)
	v_cvt_pk_bf16_f32 v105, v120, v124
	global_store_dwordx4 v[106:107], v[102:105], off nt
	v_lshl_add_u64 v[106:107], v[122:123], 0, v[76:77]
	s_nop 0
	v_cvt_pk_bf16_f32 v102, v111, v109
	v_cvt_pk_bf16_f32 v103, v113, v115
	v_cvt_pk_bf16_f32 v104, v117, v119
	v_cvt_pk_bf16_f32 v105, v121, v125
	global_store_dwordx4 v[106:107], v[102:105], off nt
	s_waitcnt lgkmcnt(0)
	s_cbranch_vccnz .LBB0_687
	s_add_i32 s12, s26, 0x8008
	s_cmp_ge_i32 s12, s25
	s_cbranch_scc1 .LBB0_686
	s_cmpk_gt_i32 s29, 0x7fef
	s_mov_b64 s[10:11], -1
	s_cbranch_scc0 .LBB0_702
	v_readlane_b32 s0, v253, 23
	s_mov_b64 s[10:11], 0
	s_nop 0
	v_mov_b32_e32 v2, s0
	ds_read_b64 v[2:3], v2
	s_add_i32 s0, s26, 8
	s_lshr_b32 s0, s0, 9
	s_add_i32 s16, s0, s14
	s_lshl_b64 s[0:1], s[16:17], 22
	s_waitcnt lgkmcnt(0)
	v_readfirstlane_b32 s5, v2
	v_readfirstlane_b32 s4, v3
	s_add_u32 s6, s5, s0
	s_addc_u32 s7, s4, s1
	s_lshl_b64 s[0:1], s[16:17], 21
	s_add_u32 s4, s15, s0
	s_addc_u32 s5, s18, s1
	s_and_b32 s16, s28, 0x3c0
	s_and_b32 s0, s27, 0x3e0
	s_lshl_b32 s1, s16, 12
	s_add_u32 s6, s6, s1
	s_addc_u32 s7, s7, 0
	s_lshl_b32 s8, s0, 2
	s_add_u32 s8, s6, s8
	s_mov_b32 s1, s17
	s_addc_u32 s9, s7, 0
	s_mov_b64 s[6:7], s[16:17]

.LBB0_1469:
	ds_write2_b32 v88, v34, v35 offset1:1
	ds_write2_b32 v88, v36, v37 offset0:2 offset1:3
	ds_write2_b32 v78, v38, v39 offset1:1
	ds_write2_b32 v89, v40, v41 offset1:1
	ds_write2_b32 v90, v42, v43 offset1:1
	ds_write2_b32 v91, v44, v45 offset1:1
	ds_write2_b32 v92, v46, v47 offset1:1
	ds_write2_b32 v93, v48, v49 offset1:1
	ds_write2_b32 v94, v54, v55 offset1:1
	ds_write2_b32 v95, v56, v57 offset1:1
	ds_write2_b32 v96, v50, v51 offset1:1
	ds_write2_b32 v97, v52, v53 offset1:1
	ds_write2_b32 v98, v62, v63 offset1:1
	ds_write2_b32 v99, v64, v65 offset1:1
	ds_write2_b32 v102, v58, v59 offset1:1
	ds_write2_b32 v103, v60, v61 offset1:1
	s_waitcnt lgkmcnt(0)
	ds_read2_b32 v[96:97], v87 offset0:33 offset1:41
	ds_read2_b32 v[98:99], v87 offset1:8
	ds_read2_b32 v[102:103], v87 offset0:66 offset1:74
	ds_read2_b32 v[104:105], v87 offset0:99 offset1:107
	ds_read2_b32 v[106:107], v87 offset0:132 offset1:140
	ds_read2_b32 v[108:109], v87 offset0:165 offset1:173
	ds_read2_b32 v[110:111], v87 offset0:198 offset1:206
	ds_read2_b32 v[112:113], v87 offset0:231 offset1:239
	v_lshl_add_u64 v[94:95], s[12:13], 0, v[100:101]
	s_waitcnt lgkmcnt(6)
	v_cvt_pk_bf16_f32 v90, v98, v96
	s_waitcnt lgkmcnt(4)
	v_cvt_pk_bf16_f32 v91, v102, v104
	s_waitcnt lgkmcnt(2)
	v_cvt_pk_bf16_f32 v92, v106, v108
	s_waitcnt lgkmcnt(0)
	v_cvt_pk_bf16_f32 v93, v110, v112
	v_lshl_add_u64 v[114:115], v[94:95], 0, v[70:71]
	global_store_dwordx4 v[114:115], v[90:93], off nt
	v_lshl_add_u64 v[114:115], v[94:95], 0, v[74:75]
	s_add_i32 s47, s47, 16
	v_cvt_pk_bf16_f32 v90, v99, v97
	v_cvt_pk_bf16_f32 v91, v103, v105
	v_cvt_pk_bf16_f32 v92, v107, v109
	v_cvt_pk_bf16_f32 v93, v111, v113
	v_lshl_add_u64 v[96:97], v[94:95], 0, v[72:73]
	global_store_dwordx4 v[96:97], v[90:93], off nt
	ds_read2_b32 v[96:97], v87 offset0:49 offset1:57
	ds_read2_b32 v[98:99], v87 offset0:16 offset1:24
	ds_read2_b32 v[102:103], v87 offset0:82 offset1:90
	ds_read2_b32 v[104:105], v87 offset0:115 offset1:123
	ds_read2_b32 v[106:107], v87 offset0:148 offset1:156
	ds_read2_b32 v[108:109], v87 offset0:181 offset1:189
	ds_read2_b32 v[110:111], v87 offset0:214 offset1:222
	ds_read2_b32 v[112:113], v87 offset0:247 offset1:255
	v_lshl_add_u64 v[94:95], v[94:95], 0, v[76:77]
	s_waitcnt lgkmcnt(6)
	v_cvt_pk_bf16_f32 v90, v98, v96
	s_waitcnt lgkmcnt(4)
	v_cvt_pk_bf16_f32 v91, v102, v104
	s_waitcnt lgkmcnt(2)
	v_cvt_pk_bf16_f32 v92, v106, v108
	s_waitcnt lgkmcnt(0)
	v_cvt_pk_bf16_f32 v93, v110, v112
	global_store_dwordx4 v[114:115], v[90:93], off nt
	s_addk_i32 s48, 0x200
	s_add_i32 s49, s49, 32
	v_cvt_pk_bf16_f32 v90, v99, v97
	v_cvt_pk_bf16_f32 v91, v103, v105
	v_cvt_pk_bf16_f32 v92, v107, v109
	v_cvt_pk_bf16_f32 v93, v111, v113
	global_store_dwordx4 v[94:95], v[90:93], off nt
	s_waitcnt lgkmcnt(0)
	s_cmp_ge_i32 s30, s46
	s_cselect_b64 s[14:15], -1, 0

.LBB0_1481:
	v_add_u32_e32 v78, 0x420, v88
	v_add_u32_e32 v89, 0x428, v88
	v_add_u32_e32 v90, 0x840, v88
	v_add_u32_e32 v91, 0x848, v88
	v_add_u32_e32 v92, 0xc60, v88
	v_add_u32_e32 v93, 0xc68, v88
	v_add_u32_e32 v94, 0x1080, v88
	v_add_u32_e32 v95, 0x1088, v88
	v_add_u32_e32 v96, 0x14a0, v88
	v_add_u32_e32 v97, 0x14a8, v88
	v_add_u32_e32 v98, 0x18c0, v88
	v_add_u32_e32 v99, 0x18c8, v88
	v_add_u32_e32 v102, 0x1ce0, v88
	v_add_u32_e32 v103, 0x1ce8, v88
	s_waitcnt vmcnt(7)
	ds_write2_b32 v88, v2, v3 offset1:1
	ds_write2_b32 v88, v4, v5 offset0:2 offset1:3
	s_waitcnt vmcnt(6)
	ds_write2_b32 v78, v6, v7 offset1:1
	ds_write2_b32 v89, v8, v9 offset1:1
	s_waitcnt vmcnt(5)
	ds_write2_b32 v90, v10, v11 offset1:1
	ds_write2_b32 v91, v12, v13 offset1:1
	s_waitcnt vmcnt(4)
	ds_write2_b32 v92, v14, v15 offset1:1
	ds_write2_b32 v93, v16, v17 offset1:1
	s_waitcnt vmcnt(3)
	ds_write2_b32 v94, v18, v19 offset1:1
	ds_write2_b32 v95, v20, v21 offset1:1
	s_waitcnt vmcnt(2)
	ds_write2_b32 v96, v22, v23 offset1:1
	ds_write2_b32 v97, v24, v25 offset1:1
	s_waitcnt vmcnt(1)
	ds_write2_b32 v98, v26, v27 offset1:1
	ds_write2_b32 v99, v28, v29 offset1:1
	s_waitcnt vmcnt(0)
	ds_write2_b32 v102, v30, v31 offset1:1
	ds_write2_b32 v103, v32, v33 offset1:1
	s_waitcnt lgkmcnt(0)
	ds_read2_b32 v[108:109], v87 offset0:33 offset1:41
	ds_read2_b32 v[110:111], v87 offset1:8
	ds_read2_b32 v[112:113], v87 offset0:66 offset1:74
	ds_read2_b32 v[114:115], v87 offset0:99 offset1:107
	ds_read2_b32 v[116:117], v87 offset0:132 offset1:140
	ds_read2_b32 v[118:119], v87 offset0:165 offset1:173
	ds_read2_b32 v[120:121], v87 offset0:198 offset1:206
	ds_read2_b32 v[122:123], v87 offset0:231 offset1:239
	v_lshlrev_b32_e32 v100, 1, v68
	v_lshl_add_u64 v[124:125], s[10:11], 0, v[100:101]
	s_waitcnt lgkmcnt(6)
	v_cvt_pk_bf16_f32 v104, v110, v108
	s_waitcnt lgkmcnt(4)
	v_cvt_pk_bf16_f32 v105, v112, v114
	s_waitcnt lgkmcnt(2)
	v_cvt_pk_bf16_f32 v106, v116, v118
	s_waitcnt lgkmcnt(0)
	v_cvt_pk_bf16_f32 v107, v120, v122
	v_lshl_add_u64 v[126:127], v[124:125], 0, v[70:71]
	global_store_dwordx4 v[126:127], v[104:107], off nt
	s_andn2_b64 vcc, exec, s[14:15]
	s_mov_b64 s[14:15], -1
	v_cvt_pk_bf16_f32 v104, v111, v109
	v_cvt_pk_bf16_f32 v105, v113, v115
	v_cvt_pk_bf16_f32 v106, v117, v119
	v_cvt_pk_bf16_f32 v107, v121, v123
	ds_read2_b32 v[110:111], v87 offset0:49 offset1:57
	ds_read2_b32 v[112:113], v87 offset0:16 offset1:24
	ds_read2_b32 v[114:115], v87 offset0:82 offset1:90
	ds_read2_b32 v[116:117], v87 offset0:115 offset1:123
	ds_read2_b32 v[118:119], v87 offset0:148 offset1:156
	ds_read2_b32 v[120:121], v87 offset0:181 offset1:189
	ds_read2_b32 v[122:123], v87 offset0:214 offset1:222
	ds_read2_b32 v[126:127], v87 offset0:247 offset1:255
	v_lshl_add_u64 v[108:109], v[124:125], 0, v[72:73]
	global_store_dwordx4 v[108:109], v[104:107], off nt
	v_lshl_add_u64 v[108:109], v[124:125], 0, v[74:75]
	s_waitcnt lgkmcnt(6)
	v_cvt_pk_bf16_f32 v104, v112, v110
	s_waitcnt lgkmcnt(4)
	v_cvt_pk_bf16_f32 v105, v114, v116
	s_waitcnt lgkmcnt(2)
	v_cvt_pk_bf16_f32 v106, v118, v120
	s_waitcnt lgkmcnt(0)
	v_cvt_pk_bf16_f32 v107, v122, v126
	global_store_dwordx4 v[108:109], v[104:107], off nt
	v_lshl_add_u64 v[108:109], v[124:125], 0, v[76:77]
	s_nop 0
	v_cvt_pk_bf16_f32 v104, v113, v111
	v_cvt_pk_bf16_f32 v105, v115, v117
	v_cvt_pk_bf16_f32 v106, v119, v121
	v_cvt_pk_bf16_f32 v107, v123, v127
	global_store_dwordx4 v[108:109], v[104:107], off nt
	s_waitcnt lgkmcnt(0)
	s_cbranch_vccnz .LBB0_1470
	s_add_i32 s30, s47, 0x8008
	s_cmp_ge_i32 s30, s46
	s_cbranch_scc1 .LBB0_1469
	s_cmpk_gt_i32 s50, 0x7fef
	s_mov_b64 s[28:29], -1
	s_cbranch_scc0 .LBB0_1485
	v_readlane_b32 s10, v253, 23
	s_mov_b64 s[28:29], 0
	s_nop 0
	v_mov_b32_e32 v2, s10
	ds_read_b64 v[2:3], v2
	s_add_i32 s10, s47, 8
	s_lshr_b32 s10, s10, 9
	s_add_i32 s16, s10, s37
	s_lshl_b64 s[10:11], s[16:17], 22
	s_waitcnt lgkmcnt(0)
	v_readfirstlane_b32 s15, v2
	v_readfirstlane_b32 s14, v3
	s_add_u32 s18, s15, s10
	s_addc_u32 s19, s14, s11
	s_lshl_b64 s[10:11], s[16:17], 21
	s_add_u32 s14, s41, s10
	s_addc_u32 s15, s42, s11
	s_and_b32 s16, s49, 0x3c0
	s_and_b32 s10, s48, 0x3e0
	s_lshl_b32 s11, s16, 12
	s_add_u32 s18, s18, s11
	s_addc_u32 s19, s19, 0
	s_lshl_b32 s26, s10, 2
	s_add_u32 s26, s18, s26
	s_mov_b32 s11, s17
	s_addc_u32 s27, s19, 0
	s_mov_b64 s[18:19], s[16:17]

.LBB0_1553:
	ds_write2_b32 v85, v32, v33 offset1:1
	ds_write2_b32 v85, v34, v35 offset0:2 offset1:3
	ds_write2_b32 v86, v36, v37 offset1:1
	ds_write2_b32 v87, v38, v39 offset1:1
	ds_write2_b32 v88, v40, v41 offset1:1
	ds_write2_b32 v89, v42, v43 offset1:1
	ds_write2_b32 v90, v44, v45 offset1:1
	ds_write2_b32 v91, v46, v47 offset1:1
	ds_write2_b32 v92, v52, v53 offset1:1
	ds_write2_b32 v93, v54, v55 offset1:1
	ds_write2_b32 v94, v48, v49 offset1:1
	ds_write2_b32 v95, v50, v51 offset1:1
	ds_write2_b32 v96, v60, v61 offset1:1
	ds_write2_b32 v97, v62, v63 offset1:1
	ds_write2_b32 v98, v56, v57 offset1:1
	ds_write2_b32 v99, v58, v59 offset1:1
	s_waitcnt lgkmcnt(0)
	ds_read2_b32 v[92:93], v84 offset0:33 offset1:41
	ds_read2_b32 v[94:95], v84 offset1:8
	ds_read2_b32 v[96:97], v84 offset0:66 offset1:74
	ds_read2_b32 v[98:99], v84 offset0:99 offset1:107
	ds_read2_b32 v[102:103], v84 offset0:132 offset1:140
	ds_read2_b32 v[104:105], v84 offset0:165 offset1:173
	ds_read2_b32 v[106:107], v84 offset0:198 offset1:206
	ds_read2_b32 v[108:109], v84 offset0:231 offset1:239
	v_lshl_add_u64 v[90:91], s[8:9], 0, v[100:101]
	s_waitcnt lgkmcnt(6)
	v_cvt_pk_bf16_f32 v86, v94, v92
	s_waitcnt lgkmcnt(4)
	v_cvt_pk_bf16_f32 v87, v96, v98
	s_waitcnt lgkmcnt(2)
	v_cvt_pk_bf16_f32 v88, v102, v104
	s_waitcnt lgkmcnt(0)
	v_cvt_pk_bf16_f32 v89, v106, v108
	v_lshl_add_u64 v[110:111], v[90:91], 0, v[68:69]
	global_store_dwordx4 v[110:111], v[86:89], off nt
	v_lshl_add_u64 v[110:111], v[90:91], 0, v[72:73]
	s_add_i32 s37, s37, 16
	v_cvt_pk_bf16_f32 v86, v95, v93
	v_cvt_pk_bf16_f32 v87, v97, v99
	v_cvt_pk_bf16_f32 v88, v103, v105
	v_cvt_pk_bf16_f32 v89, v107, v109
	v_lshl_add_u64 v[92:93], v[90:91], 0, v[70:71]
	global_store_dwordx4 v[92:93], v[86:89], off nt
	ds_read2_b32 v[92:93], v84 offset0:49 offset1:57
	ds_read2_b32 v[94:95], v84 offset0:16 offset1:24
	ds_read2_b32 v[96:97], v84 offset0:82 offset1:90
	ds_read2_b32 v[98:99], v84 offset0:115 offset1:123
	ds_read2_b32 v[102:103], v84 offset0:148 offset1:156
	ds_read2_b32 v[104:105], v84 offset0:181 offset1:189
	ds_read2_b32 v[106:107], v84 offset0:214 offset1:222
	ds_read2_b32 v[108:109], v84 offset0:247 offset1:255
	v_lshl_add_u64 v[90:91], v[90:91], 0, v[74:75]
	s_waitcnt lgkmcnt(6)
	v_cvt_pk_bf16_f32 v86, v94, v92
	s_waitcnt lgkmcnt(4)
	v_cvt_pk_bf16_f32 v87, v96, v98
	s_waitcnt lgkmcnt(2)
	v_cvt_pk_bf16_f32 v88, v102, v104
	s_waitcnt lgkmcnt(0)
	v_cvt_pk_bf16_f32 v89, v106, v108
	global_store_dwordx4 v[110:111], v[86:89], off nt
	s_addk_i32 s38, 0x200
	s_add_i32 s39, s39, 32
	v_cvt_pk_bf16_f32 v86, v95, v93
	v_cvt_pk_bf16_f32 v87, v97, v99
	v_cvt_pk_bf16_f32 v88, v103, v105
	v_cvt_pk_bf16_f32 v89, v107, v109
	global_store_dwordx4 v[90:91], v[86:89], off nt
	s_waitcnt lgkmcnt(0)
	s_cmp_ge_i32 s24, s36
	s_cselect_b64 s[10:11], -1, 0

.LBB0_1565:
	v_add_u32_e32 v86, 0x420, v85
	v_add_u32_e32 v87, 0x428, v85
	v_add_u32_e32 v88, 0x840, v85
	v_add_u32_e32 v89, 0x848, v85
	v_add_u32_e32 v90, 0xc60, v85
	v_add_u32_e32 v91, 0xc68, v85
	v_add_u32_e32 v92, 0x1080, v85
	v_add_u32_e32 v93, 0x1088, v85
	v_add_u32_e32 v94, 0x14a0, v85
	v_add_u32_e32 v95, 0x14a8, v85
	v_add_u32_e32 v96, 0x18c0, v85
	v_add_u32_e32 v97, 0x18c8, v85
	v_add_u32_e32 v98, 0x1ce0, v85
	v_add_u32_e32 v99, 0x1ce8, v85
	s_waitcnt vmcnt(7)
	ds_write2_b32 v85, v0, v1 offset1:1
	ds_write2_b32 v85, v2, v3 offset0:2 offset1:3
	s_waitcnt vmcnt(6)
	ds_write2_b32 v86, v4, v5 offset1:1
	ds_write2_b32 v87, v6, v7 offset1:1
	s_waitcnt vmcnt(5)
	ds_write2_b32 v88, v8, v9 offset1:1
	ds_write2_b32 v89, v10, v11 offset1:1
	s_waitcnt vmcnt(4)
	ds_write2_b32 v90, v12, v13 offset1:1
	ds_write2_b32 v91, v14, v15 offset1:1
	s_waitcnt vmcnt(3)
	ds_write2_b32 v92, v16, v17 offset1:1
	ds_write2_b32 v93, v18, v19 offset1:1
	s_waitcnt vmcnt(2)
	ds_write2_b32 v94, v20, v21 offset1:1
	ds_write2_b32 v95, v22, v23 offset1:1
	s_waitcnt vmcnt(1)
	ds_write2_b32 v96, v24, v25 offset1:1
	ds_write2_b32 v97, v26, v27 offset1:1
	s_waitcnt vmcnt(0)
	ds_write2_b32 v98, v28, v29 offset1:1
	ds_write2_b32 v99, v30, v31 offset1:1
	s_waitcnt lgkmcnt(0)
	ds_read2_b32 v[106:107], v84 offset0:33 offset1:41
	ds_read2_b32 v[108:109], v84 offset1:8
	ds_read2_b32 v[110:111], v84 offset0:66 offset1:74
	ds_read2_b32 v[112:113], v84 offset0:99 offset1:107
	ds_read2_b32 v[114:115], v84 offset0:132 offset1:140
	ds_read2_b32 v[116:117], v84 offset0:165 offset1:173
	ds_read2_b32 v[118:119], v84 offset0:198 offset1:206
	ds_read2_b32 v[120:121], v84 offset0:231 offset1:239
	v_lshlrev_b32_e32 v100, 1, v66
	v_lshl_add_u64 v[122:123], s[6:7], 0, v[100:101]
	s_waitcnt lgkmcnt(6)
	v_cvt_pk_bf16_f32 v102, v108, v106
	s_waitcnt lgkmcnt(4)
	v_cvt_pk_bf16_f32 v103, v110, v112
	s_waitcnt lgkmcnt(2)
	v_cvt_pk_bf16_f32 v104, v114, v116
	s_waitcnt lgkmcnt(0)
	v_cvt_pk_bf16_f32 v105, v118, v120
	v_lshl_add_u64 v[124:125], v[122:123], 0, v[68:69]
	global_store_dwordx4 v[124:125], v[102:105], off nt
	s_andn2_b64 vcc, exec, s[10:11]
	s_mov_b64 s[10:11], -1
	v_cvt_pk_bf16_f32 v102, v109, v107
	v_cvt_pk_bf16_f32 v103, v111, v113
	v_cvt_pk_bf16_f32 v104, v115, v117
	v_cvt_pk_bf16_f32 v105, v119, v121
	ds_read2_b32 v[108:109], v84 offset0:49 offset1:57
	ds_read2_b32 v[110:111], v84 offset0:16 offset1:24
	ds_read2_b32 v[112:113], v84 offset0:82 offset1:90
	ds_read2_b32 v[114:115], v84 offset0:115 offset1:123
	ds_read2_b32 v[116:117], v84 offset0:148 offset1:156
	ds_read2_b32 v[118:119], v84 offset0:181 offset1:189
	ds_read2_b32 v[120:121], v84 offset0:214 offset1:222
	ds_read2_b32 v[124:125], v84 offset0:247 offset1:255
	v_lshl_add_u64 v[106:107], v[122:123], 0, v[70:71]
	global_store_dwordx4 v[106:107], v[102:105], off nt
	v_lshl_add_u64 v[106:107], v[122:123], 0, v[72:73]
	s_waitcnt lgkmcnt(6)
	v_cvt_pk_bf16_f32 v102, v110, v108
	s_waitcnt lgkmcnt(4)
	v_cvt_pk_bf16_f32 v103, v112, v114
	s_waitcnt lgkmcnt(2)
	v_cvt_pk_bf16_f32 v104, v116, v118
	s_waitcnt lgkmcnt(0)
	v_cvt_pk_bf16_f32 v105, v120, v124
	global_store_dwordx4 v[106:107], v[102:105], off nt
	v_lshl_add_u64 v[106:107], v[122:123], 0, v[74:75]
	s_nop 0
	v_cvt_pk_bf16_f32 v102, v111, v109
	v_cvt_pk_bf16_f32 v103, v113, v115
	v_cvt_pk_bf16_f32 v104, v117, v119
	v_cvt_pk_bf16_f32 v105, v121, v125
	global_store_dwordx4 v[106:107], v[102:105], off nt
	s_waitcnt lgkmcnt(0)
	s_cbranch_vccnz .LBB0_1554
	s_add_i32 s24, s37, 0x8008
	s_cmp_ge_i32 s24, s36
	s_cbranch_scc1 .LBB0_1553
	s_cmpk_gt_i32 s40, 0x7fef
	s_mov_b64 s[18:19], -1
	s_cbranch_scc0 .LBB0_1569
	v_readlane_b32 s6, v253, 23
	s_mov_b64 s[18:19], 0
	s_nop 0
	v_mov_b32_e32 v0, s6
	ds_read_b64 v[0:1], v0
	s_add_i32 s6, s37, 8
	s_lshr_b32 s6, s6, 9
	s_add_i32 s16, s6, s28
	s_lshl_b64 s[6:7], s[16:17], 22
	s_waitcnt lgkmcnt(0)
	v_readfirstlane_b32 s11, v0
	v_readfirstlane_b32 s10, v1
	s_add_u32 s12, s11, s6
	s_addc_u32 s13, s10, s7
	s_lshl_b64 s[6:7], s[16:17], 21
	s_add_u32 s10, s29, s6
	s_addc_u32 s11, s30, s7
	s_and_b32 s16, s39, 0x3c0
	s_and_b32 s6, s38, 0x3e0
	s_lshl_b32 s7, s16, 12
	s_add_u32 s12, s12, s7
	s_addc_u32 s13, s13, 0
	s_lshl_b32 s14, s6, 2
	s_add_u32 s14, s12, s14
	s_mov_b32 s7, s17
	s_addc_u32 s15, s13, 0
	s_mov_b64 s[12:13], s[16:17]

.LBB0_1673:
	ds_write2_b32 v88, v34, v35 offset1:1
	ds_write2_b32 v88, v36, v37 offset0:2 offset1:3
	ds_write2_b32 v78, v38, v39 offset1:1
	ds_write2_b32 v89, v40, v41 offset1:1
	ds_write2_b32 v90, v42, v43 offset1:1
	ds_write2_b32 v91, v44, v45 offset1:1
	ds_write2_b32 v92, v46, v47 offset1:1
	ds_write2_b32 v93, v48, v49 offset1:1
	ds_write2_b32 v94, v54, v55 offset1:1
	ds_write2_b32 v95, v56, v57 offset1:1
	ds_write2_b32 v96, v50, v51 offset1:1
	ds_write2_b32 v97, v52, v53 offset1:1
	ds_write2_b32 v98, v62, v63 offset1:1
	ds_write2_b32 v99, v64, v65 offset1:1
	ds_write2_b32 v102, v58, v59 offset1:1
	ds_write2_b32 v103, v60, v61 offset1:1
	s_waitcnt lgkmcnt(0)
	ds_read2_b32 v[96:97], v87 offset0:33 offset1:41
	ds_read2_b32 v[98:99], v87 offset1:8
	ds_read2_b32 v[102:103], v87 offset0:66 offset1:74
	ds_read2_b32 v[104:105], v87 offset0:99 offset1:107
	ds_read2_b32 v[106:107], v87 offset0:132 offset1:140
	ds_read2_b32 v[108:109], v87 offset0:165 offset1:173
	ds_read2_b32 v[110:111], v87 offset0:198 offset1:206
	ds_read2_b32 v[112:113], v87 offset0:231 offset1:239
	v_lshl_add_u64 v[94:95], s[12:13], 0, v[100:101]
	s_waitcnt lgkmcnt(6)
	v_cvt_pk_bf16_f32 v90, v98, v96
	s_waitcnt lgkmcnt(4)
	v_cvt_pk_bf16_f32 v91, v102, v104
	s_waitcnt lgkmcnt(2)
	v_cvt_pk_bf16_f32 v92, v106, v108
	s_waitcnt lgkmcnt(0)
	v_cvt_pk_bf16_f32 v93, v110, v112
	v_lshl_add_u64 v[114:115], v[94:95], 0, v[70:71]
	global_store_dwordx4 v[114:115], v[90:93], off nt
	v_lshl_add_u64 v[114:115], v[94:95], 0, v[74:75]
	s_add_i32 s47, s47, 16
	v_cvt_pk_bf16_f32 v90, v99, v97
	v_cvt_pk_bf16_f32 v91, v103, v105
	v_cvt_pk_bf16_f32 v92, v107, v109
	v_cvt_pk_bf16_f32 v93, v111, v113
	v_lshl_add_u64 v[96:97], v[94:95], 0, v[72:73]
	global_store_dwordx4 v[96:97], v[90:93], off nt
	ds_read2_b32 v[96:97], v87 offset0:49 offset1:57
	ds_read2_b32 v[98:99], v87 offset0:16 offset1:24
	ds_read2_b32 v[102:103], v87 offset0:82 offset1:90
	ds_read2_b32 v[104:105], v87 offset0:115 offset1:123
	ds_read2_b32 v[106:107], v87 offset0:148 offset1:156
	ds_read2_b32 v[108:109], v87 offset0:181 offset1:189
	ds_read2_b32 v[110:111], v87 offset0:214 offset1:222
	ds_read2_b32 v[112:113], v87 offset0:247 offset1:255
	v_lshl_add_u64 v[94:95], v[94:95], 0, v[76:77]
	s_waitcnt lgkmcnt(6)
	v_cvt_pk_bf16_f32 v90, v98, v96
	s_waitcnt lgkmcnt(4)
	v_cvt_pk_bf16_f32 v91, v102, v104
	s_waitcnt lgkmcnt(2)
	v_cvt_pk_bf16_f32 v92, v106, v108
	s_waitcnt lgkmcnt(0)
	v_cvt_pk_bf16_f32 v93, v110, v112
	global_store_dwordx4 v[114:115], v[90:93], off nt
	s_addk_i32 s48, 0x200
	s_add_i32 s49, s49, 32
	v_cvt_pk_bf16_f32 v90, v99, v97
	v_cvt_pk_bf16_f32 v91, v103, v105
	v_cvt_pk_bf16_f32 v92, v107, v109
	v_cvt_pk_bf16_f32 v93, v111, v113
	global_store_dwordx4 v[94:95], v[90:93], off nt
	s_waitcnt lgkmcnt(0)
	s_cmp_ge_i32 s28, s46
	s_cselect_b64 s[14:15], -1, 0

.LBB0_1685:
	v_add_u32_e32 v78, 0x420, v88
	v_add_u32_e32 v89, 0x428, v88
	v_add_u32_e32 v90, 0x840, v88
	v_add_u32_e32 v91, 0x848, v88
	v_add_u32_e32 v92, 0xc60, v88
	v_add_u32_e32 v93, 0xc68, v88
	v_add_u32_e32 v94, 0x1080, v88
	v_add_u32_e32 v95, 0x1088, v88
	v_add_u32_e32 v96, 0x14a0, v88
	v_add_u32_e32 v97, 0x14a8, v88
	v_add_u32_e32 v98, 0x18c0, v88
	v_add_u32_e32 v99, 0x18c8, v88
	v_add_u32_e32 v102, 0x1ce0, v88
	v_add_u32_e32 v103, 0x1ce8, v88
	s_waitcnt vmcnt(7)
	ds_write2_b32 v88, v2, v3 offset1:1
	ds_write2_b32 v88, v4, v5 offset0:2 offset1:3
	s_waitcnt vmcnt(6)
	ds_write2_b32 v78, v6, v7 offset1:1
	ds_write2_b32 v89, v8, v9 offset1:1
	s_waitcnt vmcnt(5)
	ds_write2_b32 v90, v10, v11 offset1:1
	ds_write2_b32 v91, v12, v13 offset1:1
	s_waitcnt vmcnt(4)
	ds_write2_b32 v92, v14, v15 offset1:1
	ds_write2_b32 v93, v16, v17 offset1:1
	s_waitcnt vmcnt(3)
	ds_write2_b32 v94, v18, v19 offset1:1
	ds_write2_b32 v95, v20, v21 offset1:1
	s_waitcnt vmcnt(2)
	ds_write2_b32 v96, v22, v23 offset1:1
	ds_write2_b32 v97, v24, v25 offset1:1
	s_waitcnt vmcnt(1)
	ds_write2_b32 v98, v26, v27 offset1:1
	ds_write2_b32 v99, v28, v29 offset1:1
	s_waitcnt vmcnt(0)
	ds_write2_b32 v102, v30, v31 offset1:1
	ds_write2_b32 v103, v32, v33 offset1:1
	s_waitcnt lgkmcnt(0)
	ds_read2_b32 v[108:109], v87 offset0:33 offset1:41
	ds_read2_b32 v[110:111], v87 offset1:8
	ds_read2_b32 v[112:113], v87 offset0:66 offset1:74
	ds_read2_b32 v[114:115], v87 offset0:99 offset1:107
	ds_read2_b32 v[116:117], v87 offset0:132 offset1:140
	ds_read2_b32 v[118:119], v87 offset0:165 offset1:173
	ds_read2_b32 v[120:121], v87 offset0:198 offset1:206
	ds_read2_b32 v[122:123], v87 offset0:231 offset1:239
	v_lshlrev_b32_e32 v100, 1, v68
	v_lshl_add_u64 v[124:125], s[10:11], 0, v[100:101]
	s_waitcnt lgkmcnt(6)
	v_cvt_pk_bf16_f32 v104, v110, v108
	s_waitcnt lgkmcnt(4)
	v_cvt_pk_bf16_f32 v105, v112, v114
	s_waitcnt lgkmcnt(2)
	v_cvt_pk_bf16_f32 v106, v116, v118
	s_waitcnt lgkmcnt(0)
	v_cvt_pk_bf16_f32 v107, v120, v122
	v_lshl_add_u64 v[126:127], v[124:125], 0, v[70:71]
	global_store_dwordx4 v[126:127], v[104:107], off nt
	s_andn2_b64 vcc, exec, s[14:15]
	s_mov_b64 s[14:15], -1
	v_cvt_pk_bf16_f32 v104, v111, v109
	v_cvt_pk_bf16_f32 v105, v113, v115
	v_cvt_pk_bf16_f32 v106, v117, v119
	v_cvt_pk_bf16_f32 v107, v121, v123
	ds_read2_b32 v[110:111], v87 offset0:49 offset1:57
	ds_read2_b32 v[112:113], v87 offset0:16 offset1:24
	ds_read2_b32 v[114:115], v87 offset0:82 offset1:90
	ds_read2_b32 v[116:117], v87 offset0:115 offset1:123
	ds_read2_b32 v[118:119], v87 offset0:148 offset1:156
	ds_read2_b32 v[120:121], v87 offset0:181 offset1:189
	ds_read2_b32 v[122:123], v87 offset0:214 offset1:222
	ds_read2_b32 v[126:127], v87 offset0:247 offset1:255
	v_lshl_add_u64 v[108:109], v[124:125], 0, v[72:73]
	global_store_dwordx4 v[108:109], v[104:107], off nt
	v_lshl_add_u64 v[108:109], v[124:125], 0, v[74:75]
	s_waitcnt lgkmcnt(6)
	v_cvt_pk_bf16_f32 v104, v112, v110
	s_waitcnt lgkmcnt(4)
	v_cvt_pk_bf16_f32 v105, v114, v116
	s_waitcnt lgkmcnt(2)
	v_cvt_pk_bf16_f32 v106, v118, v120
	s_waitcnt lgkmcnt(0)
	v_cvt_pk_bf16_f32 v107, v122, v126
	global_store_dwordx4 v[108:109], v[104:107], off nt
	v_lshl_add_u64 v[108:109], v[124:125], 0, v[76:77]
	s_nop 0
	v_cvt_pk_bf16_f32 v104, v113, v111
	v_cvt_pk_bf16_f32 v105, v115, v117
	v_cvt_pk_bf16_f32 v106, v119, v121
	v_cvt_pk_bf16_f32 v107, v123, v127
	global_store_dwordx4 v[108:109], v[104:107], off nt
	s_waitcnt lgkmcnt(0)
	s_cbranch_vccnz .LBB0_1674
	s_add_i32 s28, s47, 0x8008
	s_cmp_ge_i32 s28, s46
	s_cbranch_scc1 .LBB0_1673
	s_cmpk_gt_i32 s50, 0x7fef
	s_mov_b64 s[26:27], -1
	s_cbranch_scc0 .LBB0_1689
	v_readlane_b32 s10, v253, 23
	s_mov_b64 s[26:27], 0
	s_nop 0
	v_mov_b32_e32 v2, s10
	ds_read_b64 v[2:3], v2
	s_add_i32 s10, s47, 8
	s_lshr_b32 s10, s10, 9
	s_add_i32 s16, s10, s35
	s_lshl_b64 s[10:11], s[16:17], 22
	s_waitcnt lgkmcnt(0)
	v_readfirstlane_b32 s15, v2
	v_readfirstlane_b32 s14, v3
	s_add_u32 s18, s15, s10
	s_addc_u32 s19, s14, s11
	s_lshl_b64 s[10:11], s[16:17], 21
	s_add_u32 s14, s36, s10
	s_addc_u32 s15, s37, s11
	s_and_b32 s16, s49, 0x3c0
	s_and_b32 s10, s48, 0x3e0
	s_lshl_b32 s11, s16, 12
	s_add_u32 s18, s18, s11
	s_addc_u32 s19, s19, 0
	s_lshl_b32 s24, s10, 2
	s_add_u32 s24, s18, s24
	s_mov_b32 s11, s17
	s_addc_u32 s25, s19, 0
	s_mov_b64 s[18:19], s[16:17]
